# adds P0: w_uq/w_ukv gain loads hoisted (16 together); x->XN rmsnorm rows: 4 gain chunks loaded with the row
# baseline (speedup 1.0000x reference)
.LBB0_30:
	s_mul_hi_i32 s4, s16, 0x2aaaaaab
	s_lshr_b32 s5, s4, 31
	s_ashr_i32 s4, s4, 5
	s_add_i32 s14, s4, s5
	s_ashr_i32 s15, s14, 31
	s_lshl_b64 s[4:5], s[14:15], 11
	s_add_u32 s18, s8, s4
	s_mul_i32 s4, s14, 0xffffff40
	s_addc_u32 s19, s9, s5
	s_add_i32 s15, s16, s4
	s_mul_hi_i32 s4, s15, 0x2aaaaaab
	s_lshr_b32 s5, s4, 31
	s_ashr_i32 s25, s4, 3
	s_add_i32 s25, s25, s5
	v_cndmask_b32_e64 v150, 0, 1, s[10:11]
	s_lshl_b32 s16, s25, 7
	v_mov_b32_e32 v149, 0x42800000
	v_cmp_ne_u32_e64 s[4:5], 1, v150
	s_andn2_b64 vcc, exec, s[10:11]
	v_mov_b32_e32 v150, 0x42800000
	s_cbranch_vccnz .LBB0_32
	v_or_b32_e32 v150, s16, v136
	v_ashrrev_i32_e32 v151, 31, v150
	v_lshl_add_u64 v[150:151], v[150:151], 2, s[18:19]
	global_load_dword v160, v[150:151], off
	global_load_dword v161, v[150:151], off offset:32
	global_load_dword v162, v[150:151], off offset:64
	global_load_dword v163, v[150:151], off offset:96
	global_load_dword v164, v[150:151], off offset:128
	global_load_dword v165, v[150:151], off offset:160
	global_load_dword v166, v[150:151], off offset:192
	global_load_dword v167, v[150:151], off offset:224
	global_load_dword v168, v[150:151], off offset:256
	global_load_dword v169, v[150:151], off offset:288
	global_load_dword v170, v[150:151], off offset:320
	global_load_dword v171, v[150:151], off offset:352
	global_load_dword v172, v[150:151], off offset:384
	global_load_dword v173, v[150:151], off offset:416
	global_load_dword v174, v[150:151], off offset:448
	global_load_dword v175, v[150:151], off offset:480
	s_waitcnt vmcnt(0)
	v_mul_f32_e32 v150, 0x42800000, v160
.LBB0_32:
	s_waitcnt vmcnt(15)
	v_mul_f32_e32 v126, v126, v150
	v_mul_f32_e32 v127, v127, v150
	v_mov_b32_e32 v151, 0
	v_cvt_pk_fp8_f32 v151, v126, v127
	v_mul_f32_e32 v126, v128, v150
	v_mul_f32_e32 v127, v129, v150
	s_and_b64 vcc, exec, s[4:5]
	v_cvt_pk_fp8_f32 v151, v126, v127 op_sel:[0,0,1]
	ds_write_b8 v1, v151
	v_lshrrev_b32_e32 v126, 8, v151
	ds_write_b8_d16_hi v1, v151 offset:288
	ds_write_b8 v1, v126 offset:144
	v_lshrrev_b32_e32 v126, 24, v151
	ds_write_b8 v1, v126 offset:432
	s_cbranch_vccnz .LBB0_34
	s_ashr_i32 s17, s16, 31
	v_lshl_add_u64 v[126:127], s[16:17], 0, v[136:137]
	v_lshl_add_u64 v[126:127], v[126:127], 2, s[18:19]
	v_mul_f32_e32 v149, 0x42800000, v161
.LBB0_34:
	s_waitcnt vmcnt(14)
	v_mul_f32_e32 v122, v122, v149
	v_mul_f32_e32 v123, v123, v149
	v_mov_b32_e32 v126, 0
	v_cvt_pk_fp8_f32 v126, v122, v123
	v_mul_f32_e32 v122, v124, v149
	v_mul_f32_e32 v123, v125, v149
	s_and_b64 vcc, exec, s[4:5]
	v_cvt_pk_fp8_f32 v126, v122, v123 op_sel:[0,0,1]
	v_mov_b32_e32 v123, 0x42800000
	v_lshrrev_b32_e32 v122, 8, v126
	ds_write_b8 v1, v126 offset:8
	ds_write_b8_d16_hi v1, v126 offset:296
	ds_write_b8 v1, v122 offset:152
	v_lshrrev_b32_e32 v122, 24, v126
	ds_write_b8 v1, v122 offset:440
	v_mov_b32_e32 v122, 0x42800000
	s_cbranch_vccnz .LBB0_36
	s_ashr_i32 s17, s16, 31
	v_lshl_add_u64 v[124:125], s[16:17], 0, v[136:137]
	v_lshl_add_u64 v[124:125], v[124:125], 2, s[18:19]
	v_mul_f32_e32 v123, 0x42800000, v162
.LBB0_36:
	s_waitcnt vmcnt(13)
	v_mul_f32_e32 v118, v118, v123
	v_mul_f32_e32 v119, v119, v123
	v_mov_b32_e32 v124, 0
	v_cvt_pk_fp8_f32 v124, v118, v119
	v_mul_f32_e32 v118, v120, v123
	v_mul_f32_e32 v119, v121, v123
	s_and_b64 vcc, exec, s[4:5]
	v_cvt_pk_fp8_f32 v124, v118, v119 op_sel:[0,0,1]
	ds_write_b8 v1, v124 offset:16
	v_lshrrev_b32_e32 v118, 8, v124
	ds_write_b8_d16_hi v1, v124 offset:304
	ds_write_b8 v1, v118 offset:160
	v_lshrrev_b32_e32 v118, 24, v124
	ds_write_b8 v1, v118 offset:448
	s_cbranch_vccnz .LBB0_38
	s_ashr_i32 s17, s16, 31
	v_lshl_add_u64 v[118:119], s[16:17], 0, v[136:137]
	v_lshl_add_u64 v[118:119], v[118:119], 2, s[18:19]
	v_mul_f32_e32 v122, 0x42800000, v163
.LBB0_38:
	s_waitcnt vmcnt(12)
	v_mul_f32_e32 v114, v114, v122
	v_mul_f32_e32 v115, v115, v122
	v_mov_b32_e32 v118, 0
	v_cvt_pk_fp8_f32 v118, v114, v115
	v_mul_f32_e32 v114, v116, v122
	v_mul_f32_e32 v115, v117, v122
	s_and_b64 vcc, exec, s[4:5]
	v_cvt_pk_fp8_f32 v118, v114, v115 op_sel:[0,0,1]
	v_mov_b32_e32 v115, 0x42800000
	v_lshrrev_b32_e32 v114, 8, v118
	ds_write_b8 v1, v118 offset:24
	ds_write_b8_d16_hi v1, v118 offset:312
	ds_write_b8 v1, v114 offset:168
	v_lshrrev_b32_e32 v114, 24, v118
	ds_write_b8 v1, v114 offset:456
	v_mov_b32_e32 v114, 0x42800000
	s_cbranch_vccnz .LBB0_40
	s_ashr_i32 s17, s16, 31
	v_lshl_add_u64 v[116:117], s[16:17], 0, v[136:137]
	v_lshl_add_u64 v[116:117], v[116:117], 2, s[18:19]
	v_mul_f32_e32 v115, 0x42800000, v164
.LBB0_40:
	s_waitcnt vmcnt(11)
	v_mul_f32_e32 v110, v110, v115
	v_mul_f32_e32 v111, v111, v115
	v_mov_b32_e32 v116, 0
	v_cvt_pk_fp8_f32 v116, v110, v111
	v_mul_f32_e32 v110, v112, v115
	v_mul_f32_e32 v111, v113, v115
	s_and_b64 vcc, exec, s[4:5]
	v_cvt_pk_fp8_f32 v116, v110, v111 op_sel:[0,0,1]
	ds_write_b8 v1, v116 offset:32
	v_lshrrev_b32_e32 v110, 8, v116
	ds_write_b8_d16_hi v1, v116 offset:320
	ds_write_b8 v1, v110 offset:176
	v_lshrrev_b32_e32 v110, 24, v116
	ds_write_b8 v1, v110 offset:464
	s_cbranch_vccnz .LBB0_42
	s_ashr_i32 s17, s16, 31
	v_lshl_add_u64 v[110:111], s[16:17], 0, v[136:137]
	v_lshl_add_u64 v[110:111], v[110:111], 2, s[18:19]
	v_mul_f32_e32 v114, 0x42800000, v165
.LBB0_42:
	s_waitcnt vmcnt(10)
	v_mul_f32_e32 v106, v106, v114
	v_mul_f32_e32 v107, v107, v114
	v_mov_b32_e32 v110, 0
	v_cvt_pk_fp8_f32 v110, v106, v107
	v_mul_f32_e32 v106, v108, v114
	v_mul_f32_e32 v107, v109, v114
	s_and_b64 vcc, exec, s[4:5]
	v_cvt_pk_fp8_f32 v110, v106, v107 op_sel:[0,0,1]
	v_mov_b32_e32 v107, 0x42800000
	v_lshrrev_b32_e32 v106, 8, v110
	ds_write_b8 v1, v110 offset:40
	ds_write_b8_d16_hi v1, v110 offset:328
	ds_write_b8 v1, v106 offset:184
	v_lshrrev_b32_e32 v106, 24, v110
	ds_write_b8 v1, v106 offset:472
	v_mov_b32_e32 v106, 0x42800000
	s_cbranch_vccnz .LBB0_44
	s_ashr_i32 s17, s16, 31
	v_lshl_add_u64 v[108:109], s[16:17], 0, v[136:137]
	v_lshl_add_u64 v[108:109], v[108:109], 2, s[18:19]
	v_mul_f32_e32 v107, 0x42800000, v166
.LBB0_44:
	s_waitcnt vmcnt(9)
	v_mul_f32_e32 v102, v102, v107
	v_mul_f32_e32 v103, v103, v107
	v_mov_b32_e32 v108, 0
	v_cvt_pk_fp8_f32 v108, v102, v103
	v_mul_f32_e32 v102, v104, v107
	v_mul_f32_e32 v103, v105, v107
	s_and_b64 vcc, exec, s[4:5]
	v_cvt_pk_fp8_f32 v108, v102, v103 op_sel:[0,0,1]
	ds_write_b8 v1, v108 offset:48
	v_lshrrev_b32_e32 v102, 8, v108
	ds_write_b8_d16_hi v1, v108 offset:336
	ds_write_b8 v1, v102 offset:192
	v_lshrrev_b32_e32 v102, 24, v108
	ds_write_b8 v1, v102 offset:480
	s_cbranch_vccnz .LBB0_46
	s_ashr_i32 s17, s16, 31
	v_lshl_add_u64 v[102:103], s[16:17], 0, v[136:137]
	v_lshl_add_u64 v[102:103], v[102:103], 2, s[18:19]
	v_mul_f32_e32 v106, 0x42800000, v167
.LBB0_46:
	s_waitcnt vmcnt(8)
	v_mul_f32_e32 v98, v98, v106
	v_mul_f32_e32 v99, v99, v106
	v_mov_b32_e32 v102, 0
	v_cvt_pk_fp8_f32 v102, v98, v99
	v_mul_f32_e32 v98, v100, v106
	v_mul_f32_e32 v99, v101, v106
	s_and_b64 vcc, exec, s[4:5]
	v_cvt_pk_fp8_f32 v102, v98, v99 op_sel:[0,0,1]
	v_mov_b32_e32 v99, 0x42800000
	v_lshrrev_b32_e32 v98, 8, v102
	ds_write_b8 v1, v102 offset:56
	ds_write_b8_d16_hi v1, v102 offset:344
	ds_write_b8 v1, v98 offset:200
	v_lshrrev_b32_e32 v98, 24, v102
	ds_write_b8 v1, v98 offset:488
	v_mov_b32_e32 v98, 0x42800000
	s_cbranch_vccnz .LBB0_48
	s_ashr_i32 s17, s16, 31
	v_lshl_add_u64 v[100:101], s[16:17], 0, v[136:137]
	v_lshl_add_u64 v[100:101], v[100:101], 2, s[18:19]
	v_mul_f32_e32 v99, 0x42800000, v168
.LBB0_48:
	s_waitcnt vmcnt(7)
	v_mul_f32_e32 v94, v94, v99
	v_mul_f32_e32 v95, v95, v99
	v_mov_b32_e32 v100, 0
	v_cvt_pk_fp8_f32 v100, v94, v95
	v_mul_f32_e32 v94, v96, v99
	v_mul_f32_e32 v95, v97, v99
	s_and_b64 vcc, exec, s[4:5]
	v_cvt_pk_fp8_f32 v100, v94, v95 op_sel:[0,0,1]
	ds_write_b8 v1, v100 offset:64
	v_lshrrev_b32_e32 v94, 8, v100
	ds_write_b8_d16_hi v1, v100 offset:352
	ds_write_b8 v1, v94 offset:208
	v_lshrrev_b32_e32 v94, 24, v100
	ds_write_b8 v1, v94 offset:496
	s_cbranch_vccnz .LBB0_50
	s_ashr_i32 s17, s16, 31
	v_lshl_add_u64 v[94:95], s[16:17], 0, v[136:137]
	v_lshl_add_u64 v[94:95], v[94:95], 2, s[18:19]
	v_mul_f32_e32 v98, 0x42800000, v169
.LBB0_50:
	s_waitcnt vmcnt(6)
	v_mul_f32_e32 v90, v90, v98
	v_mul_f32_e32 v91, v91, v98
	v_mov_b32_e32 v94, 0
	v_cvt_pk_fp8_f32 v94, v90, v91
	v_mul_f32_e32 v90, v92, v98
	v_mul_f32_e32 v91, v93, v98
	s_and_b64 vcc, exec, s[4:5]
	v_cvt_pk_fp8_f32 v94, v90, v91 op_sel:[0,0,1]
	v_mov_b32_e32 v91, 0x42800000
	v_lshrrev_b32_e32 v90, 8, v94
	ds_write_b8 v1, v94 offset:72
	ds_write_b8_d16_hi v1, v94 offset:360
	ds_write_b8 v1, v90 offset:216
	v_lshrrev_b32_e32 v90, 24, v94
	ds_write_b8 v1, v90 offset:504
	v_mov_b32_e32 v90, 0x42800000
	s_cbranch_vccnz .LBB0_52
	s_ashr_i32 s17, s16, 31
	v_lshl_add_u64 v[92:93], s[16:17], 0, v[136:137]
	v_lshl_add_u64 v[92:93], v[92:93], 2, s[18:19]
	v_mul_f32_e32 v91, 0x42800000, v170
.LBB0_52:
	s_waitcnt vmcnt(5)
	v_mul_f32_e32 v86, v86, v91
	v_mul_f32_e32 v87, v87, v91
	v_mov_b32_e32 v92, 0
	v_cvt_pk_fp8_f32 v92, v86, v87
	v_mul_f32_e32 v86, v88, v91
	v_mul_f32_e32 v87, v89, v91
	s_and_b64 vcc, exec, s[4:5]
	v_cvt_pk_fp8_f32 v92, v86, v87 op_sel:[0,0,1]
	ds_write_b8 v1, v92 offset:80
	v_lshrrev_b32_e32 v86, 8, v92
	ds_write_b8_d16_hi v1, v92 offset:368
	ds_write_b8 v1, v86 offset:224
	v_lshrrev_b32_e32 v86, 24, v92
	ds_write_b8 v1, v86 offset:512
	s_cbranch_vccnz .LBB0_54
	s_ashr_i32 s17, s16, 31
	v_lshl_add_u64 v[86:87], s[16:17], 0, v[136:137]
	v_lshl_add_u64 v[86:87], v[86:87], 2, s[18:19]
	v_mul_f32_e32 v90, 0x42800000, v171
.LBB0_54:
	s_waitcnt vmcnt(4)
	v_mul_f32_e32 v82, v82, v90
	v_mul_f32_e32 v83, v83, v90
	v_mov_b32_e32 v86, 0
	v_cvt_pk_fp8_f32 v86, v82, v83
	v_mul_f32_e32 v82, v84, v90
	v_mul_f32_e32 v83, v85, v90
	s_and_b64 vcc, exec, s[4:5]
	v_cvt_pk_fp8_f32 v86, v82, v83 op_sel:[0,0,1]
	v_mov_b32_e32 v83, 0x42800000
	v_lshrrev_b32_e32 v82, 8, v86
	ds_write_b8 v1, v86 offset:88
	ds_write_b8_d16_hi v1, v86 offset:376
	ds_write_b8 v1, v82 offset:232
	v_lshrrev_b32_e32 v82, 24, v86
	ds_write_b8 v1, v82 offset:520
	v_mov_b32_e32 v82, 0x42800000
	s_cbranch_vccnz .LBB0_56
	s_ashr_i32 s17, s16, 31
	v_lshl_add_u64 v[84:85], s[16:17], 0, v[136:137]
	v_lshl_add_u64 v[84:85], v[84:85], 2, s[18:19]
	v_mul_f32_e32 v83, 0x42800000, v172
.LBB0_56:
	s_waitcnt vmcnt(3)
	v_mul_f32_e32 v54, v54, v83
	v_mul_f32_e32 v55, v55, v83
	v_mov_b32_e32 v84, 0
	v_cvt_pk_fp8_f32 v84, v54, v55
	v_mul_f32_e32 v54, v56, v83
	v_mul_f32_e32 v55, v57, v83
	s_and_b64 vcc, exec, s[4:5]
	v_cvt_pk_fp8_f32 v84, v54, v55 op_sel:[0,0,1]
	ds_write_b8 v1, v84 offset:96
	v_lshrrev_b32_e32 v54, 8, v84
	ds_write_b8_d16_hi v1, v84 offset:384
	ds_write_b8 v1, v54 offset:240
	v_lshrrev_b32_e32 v54, 24, v84
	ds_write_b8 v1, v54 offset:528
	s_cbranch_vccnz .LBB0_58
	s_ashr_i32 s17, s16, 31
	v_lshl_add_u64 v[54:55], s[16:17], 0, v[136:137]
	v_lshl_add_u64 v[54:55], v[54:55], 2, s[18:19]
	v_mul_f32_e32 v82, 0x42800000, v173
.LBB0_58:
	s_waitcnt vmcnt(2)
	v_mul_f32_e32 v10, v10, v82
	v_mul_f32_e32 v11, v11, v82
	v_mov_b32_e32 v54, 0
	v_cvt_pk_fp8_f32 v54, v10, v11
	v_mul_f32_e32 v10, v12, v82
	v_mul_f32_e32 v11, v13, v82
	s_and_b64 vcc, exec, s[4:5]
	v_cvt_pk_fp8_f32 v54, v10, v11 op_sel:[0,0,1]
	ds_write_b8 v1, v54 offset:104
	v_lshrrev_b32_e32 v10, 8, v54
	ds_write_b8_d16_hi v1, v54 offset:392
	ds_write_b8 v1, v10 offset:248
	v_lshrrev_b32_e32 v10, 24, v54
	ds_write_b8 v1, v10 offset:536
	s_cbranch_vccnz .LBB0_60
	s_ashr_i32 s17, s16, 31
	v_lshl_add_u64 v[10:11], s[16:17], 0, v[136:137]
	v_lshl_add_u64 v[10:11], v[10:11], 2, s[18:19]
	v_mul_f32_e32 v10, 0x42800000, v174
	s_branch .LBB0_61

.LBB0_61:
	s_waitcnt vmcnt(1)
	v_mul_f32_e32 v6, v6, v10
	v_mul_f32_e32 v7, v7, v10
	v_mov_b32_e32 v11, 0
	v_cvt_pk_fp8_f32 v11, v6, v7
	v_mul_f32_e32 v6, v8, v10
	v_mul_f32_e32 v7, v9, v10
	s_and_b64 vcc, exec, s[10:11]
	v_cvt_pk_fp8_f32 v11, v6, v7 op_sel:[0,0,1]
	ds_write_b8 v1, v11 offset:112
	v_lshrrev_b32_e32 v6, 8, v11
	ds_write_b8_d16_hi v1, v11 offset:400
	ds_write_b8 v1, v6 offset:256
	v_lshrrev_b32_e32 v6, 24, v11
	ds_write_b8 v1, v6 offset:544
	s_cbranch_vccz .LBB0_63
	s_ashr_i32 s17, s16, 31
	v_lshl_add_u64 v[6:7], s[16:17], 0, v[136:137]
	v_lshl_add_u64 v[6:7], v[6:7], 2, s[18:19]
	v_mul_f32_e32 v6, 0x42800000, v175
	s_cbranch_execnz .LBB0_27
	s_branch .LBB0_26

.LBB0_72:
	s_ashr_i32 s4, s16, 31
	s_lshr_b32 s4, s4, 25
	s_add_i32 s17, s16, s4
	s_ashr_i32 s14, s17, 7
	s_ashr_i32 s15, s14, 31
	s_lshl_b64 s[4:5], s[14:15], 10
	s_add_u32 s18, s8, s4
	s_addc_u32 s19, s9, s5
	s_and_b32 s4, s17, 0xffffff80
	s_sub_i32 s24, s16, s4
	s_ashr_i32 s4, s24, 31
	s_lshr_b32 s4, s4, 26
	s_add_i32 s4, s24, s4
	s_ashr_i32 s25, s4, 6
	v_cndmask_b32_e64 v149, 0, 1, s[10:11]
	s_lshl_b32 s16, s25, 7
	v_mov_b32_e32 v148, 0x42800000
	v_cmp_ne_u32_e64 s[4:5], 1, v149
	s_andn2_b64 vcc, exec, s[10:11]
	v_mov_b32_e32 v149, 0x42800000
	s_cbranch_vccnz .LBB0_74
	v_or_b32_e32 v150, s16, v136
	v_ashrrev_i32_e32 v151, 31, v150
	v_lshl_add_u64 v[150:151], v[150:151], 2, s[18:19]
	global_load_dword v160, v[150:151], off
	global_load_dword v161, v[150:151], off offset:32
	global_load_dword v162, v[150:151], off offset:64
	global_load_dword v163, v[150:151], off offset:96
	global_load_dword v164, v[150:151], off offset:128
	global_load_dword v165, v[150:151], off offset:160
	global_load_dword v166, v[150:151], off offset:192
	global_load_dword v167, v[150:151], off offset:224
	global_load_dword v168, v[150:151], off offset:256
	global_load_dword v169, v[150:151], off offset:288
	global_load_dword v170, v[150:151], off offset:320
	global_load_dword v171, v[150:151], off offset:352
	global_load_dword v172, v[150:151], off offset:384
	global_load_dword v173, v[150:151], off offset:416
	global_load_dword v174, v[150:151], off offset:448
	global_load_dword v175, v[150:151], off offset:480
	s_waitcnt vmcnt(0)
	v_mul_f32_e32 v149, 0x42800000, v160
.LBB0_74:
	s_waitcnt vmcnt(15)
	v_mul_f32_e32 v126, v126, v149
	v_mul_f32_e32 v127, v127, v149
	v_mov_b32_e32 v150, 0
	v_cvt_pk_fp8_f32 v150, v126, v127
	v_mul_f32_e32 v126, v128, v149
	v_mul_f32_e32 v127, v129, v149
	s_and_b64 vcc, exec, s[4:5]
	v_cvt_pk_fp8_f32 v150, v126, v127 op_sel:[0,0,1]
	ds_write_b8 v1, v150
	v_lshrrev_b32_e32 v126, 8, v150
	ds_write_b8_d16_hi v1, v150 offset:288
	ds_write_b8 v1, v126 offset:144
	v_lshrrev_b32_e32 v126, 24, v150
	ds_write_b8 v1, v126 offset:432
	s_cbranch_vccnz .LBB0_76
	s_ashr_i32 s17, s16, 31
	v_lshl_add_u64 v[126:127], s[16:17], 0, v[136:137]
	v_lshl_add_u64 v[126:127], v[126:127], 2, s[18:19]
	v_mul_f32_e32 v148, 0x42800000, v161
.LBB0_76:
	s_waitcnt vmcnt(14)
	v_mul_f32_e32 v122, v122, v148
	v_mul_f32_e32 v123, v123, v148
	v_mov_b32_e32 v126, 0
	v_cvt_pk_fp8_f32 v126, v122, v123
	v_mul_f32_e32 v122, v124, v148
	v_mul_f32_e32 v123, v125, v148
	s_and_b64 vcc, exec, s[4:5]
	v_cvt_pk_fp8_f32 v126, v122, v123 op_sel:[0,0,1]
	v_mov_b32_e32 v123, 0x42800000
	v_lshrrev_b32_e32 v122, 8, v126
	ds_write_b8 v1, v126 offset:8
	ds_write_b8_d16_hi v1, v126 offset:296
	ds_write_b8 v1, v122 offset:152
	v_lshrrev_b32_e32 v122, 24, v126
	ds_write_b8 v1, v122 offset:440
	v_mov_b32_e32 v122, 0x42800000
	s_cbranch_vccnz .LBB0_78
	s_ashr_i32 s17, s16, 31
	v_lshl_add_u64 v[124:125], s[16:17], 0, v[136:137]
	v_lshl_add_u64 v[124:125], v[124:125], 2, s[18:19]
	v_mul_f32_e32 v123, 0x42800000, v162

.LBB0_92:
	s_waitcnt vmcnt(4)
	v_mul_f32_e32 v82, v82, v98
	v_mul_f32_e32 v83, v83, v98
	v_mov_b32_e32 v94, 0
	v_cvt_pk_fp8_f32 v94, v82, v83
	v_mul_f32_e32 v82, v84, v98
	v_mul_f32_e32 v83, v85, v98
	s_and_b64 vcc, exec, s[4:5]
	v_cvt_pk_fp8_f32 v94, v82, v83 op_sel:[0,0,1]
	v_mov_b32_e32 v83, 0x42800000
	v_lshrrev_b32_e32 v82, 8, v94
	ds_write_b8 v1, v94 offset:72
	ds_write_b8_d16_hi v1, v94 offset:360
	ds_write_b8 v1, v82 offset:216
	v_lshrrev_b32_e32 v82, 24, v94
	ds_write_b8 v1, v82 offset:504
	v_mov_b32_e32 v82, 0x42800000
	s_cbranch_vccnz .LBB0_94
	s_ashr_i32 s17, s16, 31
	v_lshl_add_u64 v[84:85], s[16:17], 0, v[136:137]
	v_lshl_add_u64 v[84:85], v[84:85], 2, s[18:19]
	v_mul_f32_e32 v83, 0x42800000, v170
.LBB0_94:
	v_mul_f32_e32 v62, v62, v83
	v_mul_f32_e32 v63, v63, v83
	v_mov_b32_e32 v84, 0
	v_cvt_pk_fp8_f32 v84, v62, v63
	v_mul_f32_e32 v62, v64, v83
	v_mul_f32_e32 v63, v65, v83
	s_and_b64 vcc, exec, s[4:5]
	v_cvt_pk_fp8_f32 v84, v62, v63 op_sel:[0,0,1]
	ds_write_b8 v1, v84 offset:80
	v_lshrrev_b32_e32 v62, 8, v84
	ds_write_b8_d16_hi v1, v84 offset:368
	ds_write_b8 v1, v62 offset:224
	v_lshrrev_b32_e32 v62, 24, v84
	ds_write_b8 v1, v62 offset:512
	s_cbranch_vccnz .LBB0_96
	s_ashr_i32 s17, s16, 31
	v_lshl_add_u64 v[62:63], s[16:17], 0, v[136:137]
	v_lshl_add_u64 v[62:63], v[62:63], 2, s[18:19]
	v_mul_f32_e32 v82, 0x42800000, v171
.LBB0_96:
	v_mul_f32_e32 v42, v42, v82
	v_mul_f32_e32 v43, v43, v82
	v_mov_b32_e32 v62, 0
	v_cvt_pk_fp8_f32 v62, v42, v43
	v_mul_f32_e32 v42, v44, v82
	v_mul_f32_e32 v43, v45, v82
	s_and_b64 vcc, exec, s[4:5]
	v_cvt_pk_fp8_f32 v62, v42, v43 op_sel:[0,0,1]
	v_mov_b32_e32 v43, 0x42800000
	v_lshrrev_b32_e32 v42, 8, v62
	ds_write_b8 v1, v62 offset:88
	ds_write_b8_d16_hi v1, v62 offset:376
	ds_write_b8 v1, v42 offset:232
	v_lshrrev_b32_e32 v42, 24, v62
	ds_write_b8 v1, v42 offset:520
	v_mov_b32_e32 v42, 0x42800000
	s_cbranch_vccnz .LBB0_98
	s_ashr_i32 s17, s16, 31
	v_lshl_add_u64 v[44:45], s[16:17], 0, v[136:137]
	v_lshl_add_u64 v[44:45], v[44:45], 2, s[18:19]
	v_mul_f32_e32 v43, 0x42800000, v172
.LBB0_98:
	s_waitcnt vmcnt(3)
	v_mul_f32_e32 v22, v22, v43
	v_mul_f32_e32 v23, v23, v43
	v_mov_b32_e32 v44, 0
	v_cvt_pk_fp8_f32 v44, v22, v23
	v_mul_f32_e32 v22, v24, v43
	v_mul_f32_e32 v23, v25, v43
	s_and_b64 vcc, exec, s[4:5]
	v_cvt_pk_fp8_f32 v44, v22, v23 op_sel:[0,0,1]
	ds_write_b8 v1, v44 offset:96
	v_lshrrev_b32_e32 v22, 8, v44
	ds_write_b8_d16_hi v1, v44 offset:384
	ds_write_b8 v1, v22 offset:240
	v_lshrrev_b32_e32 v22, 24, v44
	ds_write_b8 v1, v22 offset:528
	s_cbranch_vccnz .LBB0_100
	s_ashr_i32 s17, s16, 31
	v_lshl_add_u64 v[22:23], s[16:17], 0, v[136:137]
	v_lshl_add_u64 v[22:23], v[22:23], 2, s[18:19]
	v_mul_f32_e32 v42, 0x42800000, v173
.LBB0_100:
	s_waitcnt vmcnt(2)
	v_mul_f32_e32 v10, v10, v42
	v_mul_f32_e32 v11, v11, v42
	v_mov_b32_e32 v22, 0
	v_cvt_pk_fp8_f32 v22, v10, v11
	v_mul_f32_e32 v10, v12, v42
	v_mul_f32_e32 v11, v13, v42
	s_and_b64 vcc, exec, s[4:5]
	v_cvt_pk_fp8_f32 v22, v10, v11 op_sel:[0,0,1]
	ds_write_b8 v1, v22 offset:104
	v_lshrrev_b32_e32 v10, 8, v22
	ds_write_b8_d16_hi v1, v22 offset:392
	ds_write_b8 v1, v10 offset:248
	v_lshrrev_b32_e32 v10, 24, v22
	ds_write_b8 v1, v10 offset:536
	s_cbranch_vccnz .LBB0_102
	s_ashr_i32 s17, s16, 31
	v_lshl_add_u64 v[10:11], s[16:17], 0, v[136:137]
	v_lshl_add_u64 v[10:11], v[10:11], 2, s[18:19]
	v_mul_f32_e32 v10, 0x42800000, v174
	s_branch .LBB0_103

.LBB0_129:
	s_mov_b32 s10, 0
	s_ashr_i32 s11, s10, 31
	s_lshl_b64 s[10:11], s[10:11], 3
	s_add_u32 s10, s94, s10
	s_addc_u32 s11, s95, s11
	s_load_dwordx2 s[10:11], s[10:11], 0x0
	s_mov_b32 s0, 1
	s_ashr_i32 s1, s0, 31
	s_lshl_b64 s[0:1], s[0:1], 3
	s_waitcnt lgkmcnt(0)
	v_lshl_add_u64 v[34:35], s[10:11], 0, v[4:5]
	global_load_dwordx4 v[18:21], v[34:35], off
	global_load_dwordx4 v[22:25], v[34:35], off offset:1024
	global_load_dwordx4 v[26:29], v[34:35], off offset:2048
	global_load_dwordx4 v[30:33], v[34:35], off offset:3072
	s_add_u32 s0, s94, s0
	s_addc_u32 s1, s95, s1
	v_cmp_lt_i32_e32 vcc, v10, v9
	s_load_dwordx2 s[10:11], s[0:1], 0x0
	v_mov_b32_e32 v40, 0
	v_cndmask_b32_e32 v34, v8, v10, vcc
	v_cmp_lt_i32_e32 vcc, v11, v9
	v_lshlrev_b32_e32 v41, 2, v34
	s_add_i32 s4, s4, s2
	v_cndmask_b32_e32 v35, v8, v11, vcc
	v_cmp_lt_i32_e32 vcc, v12, v9
	v_lshlrev_b32_e32 v42, 2, v35
	v_lshl_add_u64 v[4:5], v[4:5], 0, s[8:9]
	v_cndmask_b32_e32 v36, v8, v12, vcc
	v_cmp_lt_i32_e32 vcc, v13, v9
	v_lshlrev_b32_e32 v43, 2, v36
	s_cmpk_gt_i32 s4, 0x3fff
	v_cndmask_b32_e32 v37, v8, v13, vcc
	v_lshlrev_b32_e32 v44, 2, v37
	s_waitcnt lgkmcnt(0)
	global_load_dwordx4 v[34:37], v1, s[10:11]
	global_load_dwordx4 v[160:163], v1, s[10:11] offset:1024
	global_load_dwordx4 v[164:167], v1, s[10:11] offset:2048
	global_load_dwordx4 v[168:171], v1, s[10:11] offset:3072
	v_cmp_lt_i32_e32 vcc, v14, v9
	s_waitcnt vmcnt(7)
	v_mul_f32_e32 v45, v19, v19
	v_mul_f32_e32 v46, v21, v21
	s_waitcnt vmcnt(6)
	v_mul_f32_e32 v47, v23, v23
	v_mul_f32_e32 v48, v25, v25
	s_waitcnt vmcnt(5)
	v_mul_f32_e32 v49, v27, v27
	v_mul_f32_e32 v50, v29, v29
	v_fmac_f32_e32 v45, v18, v18
	v_fmac_f32_e32 v46, v20, v20
	v_fmac_f32_e32 v47, v22, v22
	v_fmac_f32_e32 v48, v24, v24
	s_waitcnt vmcnt(4)
	v_mul_f32_e32 v51, v31, v31
	v_mul_f32_e32 v52, v33, v33
	v_fmac_f32_e32 v49, v26, v26
	v_fmac_f32_e32 v50, v28, v28
	v_add_f32_e32 v45, v45, v46
	v_add_f32_e32 v46, v47, v48
	v_fmac_f32_e32 v51, v30, v30
	v_fmac_f32_e32 v52, v32, v32
	v_add_f32_e32 v47, v49, v50
	v_add_f32_e32 v45, v45, v46
	v_add_f32_e32 v48, v51, v52
	v_add_f32_e32 v45, v45, v47
	v_add_f32_e32 v45, v45, v48
	ds_bpermute_b32 v41, v41, v45
	v_cndmask_b32_e32 v38, v8, v14, vcc
	v_lshlrev_b32_e32 v38, 2, v38
	v_cmp_lt_i32_e32 vcc, v15, v9
	s_waitcnt lgkmcnt(0)
	v_add_f32_e32 v41, v45, v41
	ds_bpermute_b32 v42, v42, v41
	v_cndmask_b32_e32 v39, v8, v15, vcc
	v_lshlrev_b32_e32 v39, 2, v39
	s_waitcnt lgkmcnt(0)
	v_add_f32_e32 v41, v41, v42
	ds_bpermute_b32 v42, v43, v41
	s_waitcnt lgkmcnt(0)
	v_add_f32_e32 v41, v41, v42
	ds_bpermute_b32 v42, v44, v41
	s_waitcnt lgkmcnt(0)
	v_add_f32_e32 v41, v41, v42
	ds_bpermute_b32 v38, v38, v41
	s_waitcnt lgkmcnt(0)
	v_add_f32_e32 v38, v41, v38
	ds_bpermute_b32 v39, v39, v38
	s_waitcnt lgkmcnt(0)
	v_add_f32_e32 v38, v38, v39
	v_fmamk_f32 v38, v38, 0x3a800000, v16
	v_mul_f32_e32 v39, 0x4f800000, v38
	v_cmp_gt_f32_e32 vcc, s3, v38
	s_nop 1
	v_cndmask_b32_e32 v38, v38, v39, vcc
	v_sqrt_f32_e32 v39, v38
	s_nop 0
	v_add_u32_e32 v41, -1, v39
	v_add_u32_e32 v42, 1, v39
	v_fma_f32 v43, -v41, v39, v38
	v_fma_f32 v44, -v42, v39, v38
	v_cmp_ge_f32_e64 s[0:1], 0, v43
	s_nop 1
	v_cndmask_b32_e64 v39, v39, v41, s[0:1]
	v_cmp_lt_f32_e64 s[0:1], 0, v44
	s_nop 1
	v_cndmask_b32_e64 v39, v39, v42, s[0:1]
	v_mul_f32_e32 v41, 0x37800000, v39
	v_cndmask_b32_e32 v39, v39, v41, vcc
	v_cmp_class_f32_e32 vcc, v38, v17
	s_nop 1
	v_cndmask_b32_e32 v38, v39, v38, vcc
	v_div_scale_f32 v39, s[0:1], v38, v38, 1.0
	v_rcp_f32_e32 v42, v39
	v_div_scale_f32 v41, vcc, 1.0, v38, 1.0
	v_fma_f32 v43, -v39, v42, 1.0
	v_fmac_f32_e32 v42, v43, v42
	v_mul_f32_e32 v43, v41, v42
	v_fma_f32 v44, -v39, v43, v41
	v_fmac_f32_e32 v43, v44, v42
	v_fma_f32 v39, -v39, v43, v41
	v_div_fmas_f32 v39, v39, v42, v43
	v_div_fixup_f32 v38, v39, v38, 1.0
	v_mul_f32_e32 v18, v18, v38
	v_mul_f32_e32 v19, v19, v38
	s_waitcnt vmcnt(3)
	v_mul_f32_e32 v18, v34, v18
	v_mul_f32_e32 v19, v35, v19
	v_cvt_pk_fp8_f32 v40, v18, v19
	v_mul_f32_e32 v20, v20, v38
	v_mul_f32_e32 v21, v21, v38
	v_mul_f32_e32 v20, v36, v20
	v_mul_f32_e32 v21, v37, v21
	v_cvt_pk_fp8_f32 v40, v20, v21 op_sel:[0,0,1]
	v_mul_f32_e32 v22, v22, v38
	v_mul_f32_e32 v23, v23, v38
	v_mov_b32_e32 v34, 0
	global_store_dword v[2:3], v40, off offset:-512
	v_mul_f32_e32 v24, v24, v38
	v_mul_f32_e32 v25, v25, v38
	s_waitcnt vmcnt(3)
	v_mov_b32_e32 v18, v160
	v_mov_b32_e32 v19, v161
	v_mov_b32_e32 v20, v162
	v_mov_b32_e32 v21, v163
	v_mul_f32_e32 v18, v18, v22
	v_mul_f32_e32 v19, v19, v23
	v_cvt_pk_fp8_f32 v34, v18, v19
	v_mul_f32_e32 v20, v20, v24
	v_mul_f32_e32 v21, v21, v25
	v_mul_f32_e32 v23, v26, v38
	v_cvt_pk_fp8_f32 v34, v20, v21 op_sel:[0,0,1]
	v_mul_f32_e32 v24, v27, v38
	v_mov_b32_e32 v22, 0
	v_mul_f32_e32 v25, v28, v38
	global_store_dword v[2:3], v34, off offset:-256
	v_mul_f32_e32 v26, v29, v38
	s_waitcnt vmcnt(3)
	v_mov_b32_e32 v18, v164
	v_mov_b32_e32 v19, v165
	v_mov_b32_e32 v20, v166
	v_mov_b32_e32 v21, v167
	v_mul_f32_e32 v18, v23, v18
	v_mul_f32_e32 v19, v24, v19
	v_cvt_pk_fp8_f32 v22, v18, v19
	v_mul_f32_e32 v20, v25, v20
	v_mul_f32_e32 v18, v26, v21
	v_mul_f32_e32 v23, v30, v38
	v_cvt_pk_fp8_f32 v22, v20, v18 op_sel:[0,0,1]
	v_mul_f32_e32 v24, v31, v38
	v_mul_f32_e32 v25, v32, v38
	v_mul_f32_e32 v26, v33, v38
	global_store_dword v[2:3], v22, off
	v_mov_b32_e32 v22, 0
	s_waitcnt vmcnt(3)
	v_mov_b32_e32 v18, v168
	v_mov_b32_e32 v19, v169
	v_mov_b32_e32 v20, v170
	v_mov_b32_e32 v21, v171
	v_mul_f32_e32 v18, v23, v18
	v_mul_f32_e32 v19, v24, v19
	v_cvt_pk_fp8_f32 v22, v18, v19
	v_mul_f32_e32 v18, v25, v20
	v_mul_f32_e32 v19, v26, v21
	v_cvt_pk_fp8_f32 v22, v18, v19 op_sel:[0,0,1]
	global_store_dword v[2:3], v22, off offset:256
	v_lshl_add_u64 v[2:3], v[2:3], 0, s[6:7]
	s_cbranch_scc0 .LBB0_129
